# v71 + P10: histogram cleared with 16 x ds_write_b128 per thread; boundary-bin rank loop double-buffers its candidate reads
# speedup vs baseline: 1.0083x; 1.0083x over previous
.LBB0_1113:
	s_or_b64 exec, exec, s[0:1]
	v_cmp_gt_i32_e32 vcc, s42, v16
	s_and_saveexec_b64 s[50:51], vcc
	s_cbranch_execz .LBB0_1116
	v_readlane_b32 s0, v254, 56
	v_mov_b64_e32 v[4:5], 0
	v_mov_b64_e32 v[6:7], 0
	s_waitcnt lgkmcnt(0)
	s_nop 0
	v_add_u32_e32 v0, s0, v150
	v_lshlrev_b32_e32 v0, 4, v0
	v_add_u32_e32 v0, 0x6000, v0
	v_add_u32_e32 v1, 0x10000, v0
	ds_write_b128 v0, v[4:7]
	ds_write_b128 v0, v[4:7] offset:8192
	ds_write_b128 v0, v[4:7] offset:16384
	ds_write_b128 v0, v[4:7] offset:24576
	ds_write_b128 v0, v[4:7] offset:32768
	ds_write_b128 v0, v[4:7] offset:40960
	ds_write_b128 v0, v[4:7] offset:49152
	ds_write_b128 v0, v[4:7] offset:57344
	ds_write_b128 v1, v[4:7]
	ds_write_b128 v1, v[4:7] offset:8192
	ds_write_b128 v1, v[4:7] offset:16384
	ds_write_b128 v1, v[4:7] offset:24576
	ds_write_b128 v1, v[4:7] offset:32768
	ds_write_b128 v1, v[4:7] offset:40960
	ds_write_b128 v1, v[4:7] offset:49152
	ds_write_b128 v1, v[4:7] offset:57344

.LBB0_1379:
	v_or_b32_e32 v7, s25, v147
	v_lshl_add_u32 v6, v7, 2, v3
	ds_read_b32 v6, v6
	v_mov_b32_e32 v9, 0
	v_mov_b32_e32 v8, v5
	s_mov_b32 s0, 0
	v_add_u32_e32 v10, -16, v8
	ds_read_b128 v[10:13], v10
	ds_read_b128 v[14:17], v8
	v_add_u32_e32 v8, 32, v8
.LBB0_1380:
	v_add_u32_e32 v18, -16, v8
	ds_read_b128 v[18:21], v18
	ds_read_b128 v[22:25], v8
	v_add_u32_e32 v8, 32, v8
	s_add_i32 s0, s0, 8
	s_cmp_ge_i32 s0, s24
	s_waitcnt lgkmcnt(2)
	v_cmp_gt_u32_e32 vcc, v11, v6
	s_nop 1
	v_cndmask_b32_e64 v11, 0, 1, vcc
	v_cmp_gt_u32_e32 vcc, v12, v6
	s_nop 1
	v_cndmask_b32_e64 v12, 0, 1, vcc
	v_cmp_gt_u32_e32 vcc, v14, v6
	s_nop 1
	v_cndmask_b32_e64 v14, 0, 1, vcc
	v_cmp_gt_u32_e32 vcc, v16, v6
	s_nop 1
	v_cndmask_b32_e64 v16, 0, 1, vcc
	v_cmp_gt_u32_e32 vcc, v10, v6
	s_nop 1
	v_addc_co_u32_e32 v9, vcc, v9, v11, vcc
	v_cmp_gt_u32_e32 vcc, v13, v6
	s_nop 1
	v_addc_co_u32_e32 v9, vcc, v9, v12, vcc
	v_cmp_gt_u32_e32 vcc, v15, v6
	s_nop 1
	v_addc_co_u32_e32 v9, vcc, v9, v14, vcc
	v_cmp_gt_u32_e32 vcc, v17, v6
	s_nop 1
	v_addc_co_u32_e32 v9, vcc, v9, v16, vcc
	s_cbranch_scc1 .Lrs_exit
	v_add_u32_e32 v10, -16, v8
	ds_read_b128 v[10:13], v10
	ds_read_b128 v[14:17], v8
	v_add_u32_e32 v8, 32, v8
	s_add_i32 s0, s0, 8
	s_cmp_ge_i32 s0, s24
	s_waitcnt lgkmcnt(2)
	v_cmp_gt_u32_e32 vcc, v19, v6
	s_nop 1
	v_cndmask_b32_e64 v19, 0, 1, vcc
	v_cmp_gt_u32_e32 vcc, v20, v6
	s_nop 1
	v_cndmask_b32_e64 v20, 0, 1, vcc
	v_cmp_gt_u32_e32 vcc, v22, v6
	s_nop 1
	v_cndmask_b32_e64 v22, 0, 1, vcc
	v_cmp_gt_u32_e32 vcc, v24, v6
	s_nop 1
	v_cndmask_b32_e64 v24, 0, 1, vcc
	v_cmp_gt_u32_e32 vcc, v18, v6
	s_nop 1
	v_addc_co_u32_e32 v9, vcc, v9, v19, vcc
	v_cmp_gt_u32_e32 vcc, v21, v6
	s_nop 1
	v_addc_co_u32_e32 v9, vcc, v9, v20, vcc
	v_cmp_gt_u32_e32 vcc, v23, v6
	s_nop 1
	v_addc_co_u32_e32 v9, vcc, v9, v22, vcc
	v_cmp_gt_u32_e32 vcc, v25, v6
	s_nop 1
	v_addc_co_u32_e32 v9, vcc, v9, v24, vcc
	s_cbranch_scc0 .LBB0_1380
.Lrs_exit:
	v_cmp_lt_i32_e32 vcc, v7, v0
	v_add_u32_e32 v7, v9, v2
	v_cmp_lt_i32_e64 s[50:51], v9, v1
	v_cmp_gt_i32_e64 s[52:53], s48, v7
	s_and_b64 s[0:1], s[50:51], s[52:53]
	s_and_b64 s[26:27], vcc, s[0:1]
	s_and_saveexec_b64 s[0:1], s[26:27]
	s_cbranch_execz .LBB0_1378
	v_xor_b32_e32 v6, -1, v6
	v_lshl_add_u32 v7, v7, 1, v4
	ds_write_b16 v7, v6 offset:24576
	s_branch .LBB0_1378
